# P2 rope-key mini-GEMM: operand loads issued six K-steps ahead in a 7-slot register ring (compiler had sunk each load to 1-2 steps before its MFMA)
# baseline (speedup 1.0000x reference)
; __global__ void __launch_bounds__(512, 2) fwd_kernel(Params p) {
;     ...
;                 const bf16_t* hr = Hb + (size_t)(blk * 64 + tt * 32 + j) * DM + kq * 512 + hh * 8;
;                 const bf16_t* w0 = WkrT + (size_t)j * DM + kq * 512 + hh * 8; const bf16_t* w1 = w0 + (size_t)32 * DM;
;                 f32x16 a0 = {}, a1 = {};
;                 bf16x8 hb[32], b0[2][4], b1[2][4];
; #pragma unroll
;                 for (int i = 0; i < 32; ++i) hb[i] = *(const bf16x8*)(hr + i * 16);
; #pragma unroll
;                 for (int i = 0; i < 4; ++i) { b0[0][i] = *(const bf16x8*)(w0 + i * 16); b1[0][i] = *(const bf16x8*)(w1 + i * 16); }
; #pragma unroll
;                 for (int ch = 0; ch < 8; ++ch) {
;                     if (ch + 1 < 8) {
; #pragma unroll
;                         for (int i = 0; i < 4; ++i) { b0[(ch + 1) & 1][i] = *(const bf16x8*)(w0 + (ch + 1) * 64 + i * 16); b1[(ch + 1) & 1][i] = *(const bf16x8*)(w1 + (ch + 1) * 64 + i * 16); } }
; #pragma unroll
;                     for (int i = 0; i < 4; ++i) { a0 = __builtin_amdgcn_mfma_f32_32x32x16_bf16(b0[ch & 1][i], hb[ch * 4 + i], a0, 0, 0, 0); a1 = __builtin_amdgcn_mfma_f32_32x32x16_bf16(b1[ch & 1][i], hb[ch * 4 + i], a1, 0, 0, 0); }
;                 }
.LBB0_230:
	v_lshl_or_b32 v4, s45, 6, v109
	v_ashrrev_i32_e32 v5, 31, v4
	v_lshlrev_b64 v[4:5], 12, v[4:5]
	v_lshl_add_u64 v[112:113], v[34:35], 0, v[4:5]
	global_load_dwordx4 v[160:163], v[38:39], off
	global_load_dwordx4 v[164:167], v[112:113], off
	global_load_dwordx4 v[168:171], v[40:41], off
	global_load_dwordx4 v[172:175], v[38:39], off offset:32
	global_load_dwordx4 v[176:179], v[112:113], off offset:32
	global_load_dwordx4 v[180:183], v[46:47], off
	global_load_dwordx4 v[184:187], v[38:39], off offset:64
	global_load_dwordx4 v[188:191], v[112:113], off offset:64
	global_load_dwordx4 v[192:195], v[48:49], off
	global_load_dwordx4 v[196:199], v[38:39], off offset:96
	global_load_dwordx4 v[200:203], v[112:113], off offset:96
	global_load_dwordx4 v[204:207], v[50:51], off
	global_load_dwordx4 v[208:211], v[38:39], off offset:128
	global_load_dwordx4 v[212:215], v[112:113], off offset:128
	global_load_dwordx4 v[216:219], v[52:53], off
	global_load_dwordx4 v[140:143], v[38:39], off offset:160
	global_load_dwordx4 v[144:147], v[112:113], off offset:160
	global_load_dwordx4 v[148:151], v[54:55], off
	s_ashr_i32 s27, s26, 31
	s_lshl_b64 s[10:11], s[26:27], 8
	s_lshl_b64 s[52:53], s[26:27], 2
	global_load_dwordx4 v[152:155], v[38:39], off offset:192
	global_load_dwordx4 v[156:159], v[112:113], off offset:192
	global_load_dwordx4 v[230:233], v[56:57], off
	s_waitcnt vmcnt(18)
	v_mfma_f32_32x32x16_bf16 v[0:15], v[160:163], v[164:167], 0
	v_mfma_f32_32x32x16_bf16 v[16:31], v[168:171], v[164:167], 0
	global_load_dwordx4 v[160:163], v[38:39], off offset:224
	global_load_dwordx4 v[164:167], v[112:113], off offset:224
	global_load_dwordx4 v[168:171], v[58:59], off
	s_waitcnt vmcnt(18)
	v_mfma_f32_32x32x16_bf16 v[0:15], v[172:175], v[176:179], v[0:15]
	v_mfma_f32_32x32x16_bf16 v[16:31], v[180:183], v[176:179], v[16:31]
	global_load_dwordx4 v[172:175], v[38:39], off offset:256
	global_load_dwordx4 v[176:179], v[112:113], off offset:256
	global_load_dwordx4 v[180:183], v[60:61], off
	s_waitcnt vmcnt(18)
	v_mfma_f32_32x32x16_bf16 v[0:15], v[184:187], v[188:191], v[0:15]
	v_mfma_f32_32x32x16_bf16 v[16:31], v[192:195], v[188:191], v[16:31]
	global_load_dwordx4 v[184:187], v[38:39], off offset:288
	global_load_dwordx4 v[188:191], v[112:113], off offset:288
	global_load_dwordx4 v[192:195], v[62:63], off
	s_waitcnt vmcnt(18)
	v_mfma_f32_32x32x16_bf16 v[0:15], v[196:199], v[200:203], v[0:15]
	v_mfma_f32_32x32x16_bf16 v[16:31], v[204:207], v[200:203], v[16:31]
	global_load_dwordx4 v[196:199], v[38:39], off offset:320
	global_load_dwordx4 v[200:203], v[112:113], off offset:320
	global_load_dwordx4 v[204:207], v[64:65], off
	s_waitcnt vmcnt(18)
	v_mfma_f32_32x32x16_bf16 v[0:15], v[208:211], v[212:215], v[0:15]
	v_mfma_f32_32x32x16_bf16 v[16:31], v[216:219], v[212:215], v[16:31]
	global_load_dwordx4 v[208:211], v[38:39], off offset:352
	global_load_dwordx4 v[212:215], v[112:113], off offset:352
	global_load_dwordx4 v[216:219], v[66:67], off
	s_waitcnt vmcnt(18)
	v_mfma_f32_32x32x16_bf16 v[0:15], v[140:143], v[144:147], v[0:15]
	v_mfma_f32_32x32x16_bf16 v[16:31], v[148:151], v[144:147], v[16:31]
	global_load_dwordx4 v[140:143], v[38:39], off offset:384
	global_load_dwordx4 v[144:147], v[112:113], off offset:384
	global_load_dwordx4 v[148:151], v[68:69], off
	s_waitcnt vmcnt(18)
	v_mfma_f32_32x32x16_bf16 v[0:15], v[152:155], v[156:159], v[0:15]
	v_mfma_f32_32x32x16_bf16 v[16:31], v[230:233], v[156:159], v[16:31]
	global_load_dwordx4 v[152:155], v[38:39], off offset:416
	global_load_dwordx4 v[156:159], v[112:113], off offset:416
	global_load_dwordx4 v[230:233], v[70:71], off
	s_waitcnt vmcnt(18)
	v_mfma_f32_32x32x16_bf16 v[0:15], v[160:163], v[164:167], v[0:15]
	v_mfma_f32_32x32x16_bf16 v[16:31], v[168:171], v[164:167], v[16:31]
	global_load_dwordx4 v[160:163], v[38:39], off offset:448
	global_load_dwordx4 v[164:167], v[112:113], off offset:448
	global_load_dwordx4 v[168:171], v[72:73], off
	s_waitcnt vmcnt(18)
	v_mfma_f32_32x32x16_bf16 v[0:15], v[172:175], v[176:179], v[0:15]
	v_mfma_f32_32x32x16_bf16 v[16:31], v[180:183], v[176:179], v[16:31]
	global_load_dwordx4 v[172:175], v[38:39], off offset:480
	global_load_dwordx4 v[176:179], v[112:113], off offset:480
	global_load_dwordx4 v[180:183], v[74:75], off
	s_waitcnt vmcnt(18)
	v_mfma_f32_32x32x16_bf16 v[0:15], v[184:187], v[188:191], v[0:15]
	v_mfma_f32_32x32x16_bf16 v[16:31], v[192:195], v[188:191], v[16:31]
	global_load_dwordx4 v[184:187], v[38:39], off offset:512
	global_load_dwordx4 v[188:191], v[112:113], off offset:512
	global_load_dwordx4 v[192:195], v[76:77], off
	s_waitcnt vmcnt(18)
	v_mfma_f32_32x32x16_bf16 v[0:15], v[196:199], v[200:203], v[0:15]
	v_mfma_f32_32x32x16_bf16 v[16:31], v[204:207], v[200:203], v[16:31]
	global_load_dwordx4 v[196:199], v[38:39], off offset:544
	global_load_dwordx4 v[200:203], v[112:113], off offset:544
	global_load_dwordx4 v[204:207], v[78:79], off
	s_waitcnt vmcnt(18)
	v_mfma_f32_32x32x16_bf16 v[0:15], v[208:211], v[212:215], v[0:15]
	v_mfma_f32_32x32x16_bf16 v[16:31], v[216:219], v[212:215], v[16:31]
	global_load_dwordx4 v[208:211], v[38:39], off offset:576
	global_load_dwordx4 v[212:215], v[112:113], off offset:576
	global_load_dwordx4 v[216:219], v[80:81], off
	s_waitcnt vmcnt(18)
	v_mfma_f32_32x32x16_bf16 v[0:15], v[140:143], v[144:147], v[0:15]
	v_mfma_f32_32x32x16_bf16 v[16:31], v[148:151], v[144:147], v[16:31]
	global_load_dwordx4 v[140:143], v[38:39], off offset:608
	global_load_dwordx4 v[144:147], v[112:113], off offset:608
	global_load_dwordx4 v[148:151], v[82:83], off
	s_waitcnt vmcnt(18)
; #define LAS __attribute__((address_space(3)))
; __global__ void __launch_bounds__(512, 2) fwd_kernel(Params p) {
;     ...
;                 for (int ch = 0; ch < 8; ++ch) {
;                     if (ch + 1 < 8) {
; #pragma unroll
;                         for (int i = 0; i < 4; ++i) { b0[(ch + 1) & 1][i] = *(const bf16x8*)(w0 + (ch + 1) * 64 + i * 16); b1[(ch + 1) & 1][i] = *(const bf16x8*)(w1 + (ch + 1) * 64 + i * 16); } }
; #pragma unroll
;                     for (int i = 0; i < 4; ++i) { a0 = __builtin_amdgcn_mfma_f32_32x32x16_bf16(b0[ch & 1][i], hb[ch * 4 + i], a0, 0, 0, 0); a1 = __builtin_amdgcn_mfma_f32_32x32x16_bf16(b1[ch & 1][i], hb[ch * 4 + i], a1, 0, 0, 0); }
;                 }
;                 LAS float* pp = zk + (kq * 64 + tt * 32 + j) * 65;
; #pragma unroll
;                 for (int r = 0; r < 16; ++r) { const int c = (r & 3) + 8 * (r >> 2) + 4 * hh; pp[c] = a0[r]; pp[32 + c] = a1[r]; }
;             }
;             __syncthreads();
;             const float inv_freq = powf(10000.0f, -(float)(2 * (lane & 31)) / 64.0f);
; #pragma unroll 1
;             for (int tl = wave * 8; tl < wave * 8 + 8; ++tl) {
;                 const int m = blk * 64 + tl;
;                 const bf16_t* zr = Zb + (size_t)m * ZLD;
;                 {
;                     const u32x2 zq = *(const u32x2*)(Z8 + (size_t)m * 1024 + lane * 8), zkv = *(const u32x2*)(Z8 + (size_t)m * 1024 + 512 + lane * 8);
	v_mfma_f32_32x32x16_bf16 v[0:15], v[152:155], v[156:159], v[0:15]
	v_mfma_f32_32x32x16_bf16 v[16:31], v[230:233], v[156:159], v[16:31]
	global_load_dwordx4 v[152:155], v[38:39], off offset:640
	global_load_dwordx4 v[156:159], v[112:113], off offset:640
	global_load_dwordx4 v[230:233], v[84:85], off
	s_waitcnt vmcnt(18)
	v_mfma_f32_32x32x16_bf16 v[0:15], v[160:163], v[164:167], v[0:15]
	v_mfma_f32_32x32x16_bf16 v[16:31], v[168:171], v[164:167], v[16:31]
	global_load_dwordx4 v[160:163], v[38:39], off offset:672
	global_load_dwordx4 v[164:167], v[112:113], off offset:672
	global_load_dwordx4 v[168:171], v[86:87], off
	s_waitcnt vmcnt(18)
	v_mfma_f32_32x32x16_bf16 v[0:15], v[172:175], v[176:179], v[0:15]
	v_mfma_f32_32x32x16_bf16 v[16:31], v[180:183], v[176:179], v[16:31]
	global_load_dwordx4 v[172:175], v[38:39], off offset:704
	global_load_dwordx4 v[176:179], v[112:113], off offset:704
	global_load_dwordx4 v[180:183], v[88:89], off
	s_waitcnt vmcnt(18)
	v_mfma_f32_32x32x16_bf16 v[0:15], v[184:187], v[188:191], v[0:15]
	v_mfma_f32_32x32x16_bf16 v[16:31], v[192:195], v[188:191], v[16:31]
	global_load_dwordx4 v[184:187], v[38:39], off offset:736
	global_load_dwordx4 v[188:191], v[112:113], off offset:736
	global_load_dwordx4 v[192:195], v[90:91], off
	s_waitcnt vmcnt(18)
	v_mfma_f32_32x32x16_bf16 v[0:15], v[196:199], v[200:203], v[0:15]
	v_mfma_f32_32x32x16_bf16 v[16:31], v[204:207], v[200:203], v[16:31]
	global_load_dwordx4 v[196:199], v[38:39], off offset:768
	global_load_dwordx4 v[200:203], v[112:113], off offset:768
	global_load_dwordx4 v[204:207], v[92:93], off
	s_waitcnt vmcnt(18)
	v_mfma_f32_32x32x16_bf16 v[0:15], v[208:211], v[212:215], v[0:15]
	v_mfma_f32_32x32x16_bf16 v[16:31], v[216:219], v[212:215], v[16:31]
	global_load_dwordx4 v[208:211], v[38:39], off offset:800
	global_load_dwordx4 v[212:215], v[112:113], off offset:800
	global_load_dwordx4 v[216:219], v[94:95], off
	s_waitcnt vmcnt(18)
	v_mfma_f32_32x32x16_bf16 v[0:15], v[140:143], v[144:147], v[0:15]
	v_mfma_f32_32x32x16_bf16 v[16:31], v[148:151], v[144:147], v[16:31]
	global_load_dwordx4 v[140:143], v[38:39], off offset:832
	global_load_dwordx4 v[144:147], v[112:113], off offset:832
	global_load_dwordx4 v[148:151], v[96:97], off
	s_waitcnt vmcnt(18)
	v_mfma_f32_32x32x16_bf16 v[0:15], v[152:155], v[156:159], v[0:15]
	v_mfma_f32_32x32x16_bf16 v[16:31], v[230:233], v[156:159], v[16:31]
	global_load_dwordx4 v[152:155], v[38:39], off offset:864
	global_load_dwordx4 v[156:159], v[112:113], off offset:864
	global_load_dwordx4 v[230:233], v[98:99], off
	s_waitcnt vmcnt(18)
	v_mfma_f32_32x32x16_bf16 v[0:15], v[160:163], v[164:167], v[0:15]
	v_mfma_f32_32x32x16_bf16 v[16:31], v[168:171], v[164:167], v[16:31]
	global_load_dwordx4 v[160:163], v[38:39], off offset:896
	global_load_dwordx4 v[164:167], v[112:113], off offset:896
	global_load_dwordx4 v[168:171], v[100:101], off
	s_waitcnt vmcnt(18)
	v_mfma_f32_32x32x16_bf16 v[0:15], v[172:175], v[176:179], v[0:15]
	v_mfma_f32_32x32x16_bf16 v[16:31], v[180:183], v[176:179], v[16:31]
	global_load_dwordx4 v[172:175], v[38:39], off offset:928
	global_load_dwordx4 v[176:179], v[112:113], off offset:928
	global_load_dwordx4 v[180:183], v[102:103], off
	s_waitcnt vmcnt(18)
	v_mfma_f32_32x32x16_bf16 v[0:15], v[184:187], v[188:191], v[0:15]
	v_mfma_f32_32x32x16_bf16 v[16:31], v[192:195], v[188:191], v[16:31]
	global_load_dwordx4 v[184:187], v[38:39], off offset:960
	global_load_dwordx4 v[188:191], v[112:113], off offset:960
	global_load_dwordx4 v[192:195], v[104:105], off
	s_waitcnt vmcnt(18)
	v_mfma_f32_32x32x16_bf16 v[0:15], v[196:199], v[200:203], v[0:15]
	v_mfma_f32_32x32x16_bf16 v[16:31], v[204:207], v[200:203], v[16:31]
	global_load_dwordx4 v[196:199], v[38:39], off offset:992
	global_load_dwordx4 v[200:203], v[112:113], off offset:992
	global_load_dwordx4 v[204:207], v[106:107], off
	s_waitcnt vmcnt(18)
	v_mfma_f32_32x32x16_bf16 v[0:15], v[208:211], v[212:215], v[0:15]
	v_mfma_f32_32x32x16_bf16 v[16:31], v[216:219], v[212:215], v[16:31]
	s_waitcnt vmcnt(15)
	v_mfma_f32_32x32x16_bf16 v[0:15], v[140:143], v[144:147], v[0:15]
	v_mfma_f32_32x32x16_bf16 v[16:31], v[148:151], v[144:147], v[16:31]
	s_waitcnt vmcnt(12)
	v_mfma_f32_32x32x16_bf16 v[0:15], v[152:155], v[156:159], v[0:15]
	v_mfma_f32_32x32x16_bf16 v[16:31], v[230:233], v[156:159], v[16:31]
	s_waitcnt vmcnt(9)
	v_mfma_f32_32x32x16_bf16 v[0:15], v[160:163], v[164:167], v[0:15]
	v_mfma_f32_32x32x16_bf16 v[16:31], v[168:171], v[164:167], v[16:31]
	s_waitcnt vmcnt(6)
	v_mfma_f32_32x32x16_bf16 v[0:15], v[172:175], v[176:179], v[0:15]
	v_mfma_f32_32x32x16_bf16 v[16:31], v[180:183], v[176:179], v[16:31]
	s_waitcnt vmcnt(3)
	v_mfma_f32_32x32x16_bf16 v[0:15], v[184:187], v[188:191], v[0:15]
	v_mfma_f32_32x32x16_bf16 v[16:31], v[192:195], v[188:191], v[16:31]
	v_mov_b32_e32 v113, s11
	v_or_b32_e32 v112, s10, v42
	s_lshl_b64 s[10:11], s[26:27], 6
	v_mov_b32_e32 v115, s11
	v_or_b32_e32 v114, s10, v108
	s_lshl_b64 s[10:11], s[26:27], 10
	v_lshl_add_u64 v[116:117], v[32:33], 0, s[10:11]
	s_mov_b32 s27, 0
	s_waitcnt vmcnt(0)
	v_mfma_f32_32x32x16_bf16 v[0:15], v[196:199], v[200:203], v[0:15]
	v_mfma_f32_32x32x16_bf16 v[16:31], v[204:207], v[200:203], v[16:31]
	s_nop 11
	ds_write2_b32 v124, v0, v1 offset1:1
	ds_write2_b32 v124, v16, v17 offset0:32 offset1:33
	ds_write2_b32 v124, v2, v3 offset0:2 offset1:3
	ds_write2_b32 v124, v18, v19 offset0:34 offset1:35
	ds_write2_b32 v124, v4, v5 offset0:8 offset1:9
	ds_write2_b32 v124, v20, v21 offset0:40 offset1:41
	ds_write2_b32 v124, v6, v7 offset0:10 offset1:11
	ds_write2_b32 v124, v22, v23 offset0:42 offset1:43
	ds_write2_b32 v124, v8, v9 offset0:16 offset1:17
	ds_write2_b32 v124, v24, v25 offset0:48 offset1:49
	ds_write2_b32 v124, v10, v11 offset0:18 offset1:19
	ds_write2_b32 v124, v26, v27 offset0:50 offset1:51
	ds_write2_b32 v124, v12, v13 offset0:24 offset1:25
	ds_write2_b32 v124, v28, v29 offset0:56 offset1:57
	ds_write2_b32 v124, v14, v15 offset0:26 offset1:27
	ds_write2_b32 v124, v30, v31 offset0:58 offset1:59
	s_waitcnt lgkmcnt(0)
	v_lshl_add_u64 v[226:227], s[28:29], 0, v[116:117]
	v_add_co_u32_e32 v226, vcc, 0x25800000, v226
	s_add_u32 s10, s24, s52
	s_addc_u32 s11, s25, s53
	v_addc_co_u32_e32 v227, vcc, 0, v227, vcc
	global_load_dwordx2 v[220:221], v[226:227], off
	global_load_dwordx2 v[222:223], v[226:227], off offset:512
	global_load_dword v224, v37, s[10:11]
	global_load_dword v228, v[44:45], off
	global_load_dword v229, v[44:45], off offset:128
	s_barrier
	s_waitcnt vmcnt(0)
	s_branch .LBB0_232
